# baseline (speedup 1.0000x reference)
.LBB16_7:
	s_setprio 3
	s_waitcnt vmcnt(0)
	s_load_dwordx4 s[8:11], s[0:1], 0x50
	s_waitcnt vmcnt(4)
	v_mul_u32_u24_e32 v76, 0x2800, v11
	s_load_dword s24, s[0:1], 0x6c
	s_load_dwordx2 s[0:1], s[0:1], 0x40
	v_ashrrev_i32_e32 v11, 31, v10
	v_mov_b32_e32 v0, s6
	v_lshrrev_b32_e32 v4, 2, v25
	v_accvgpr_read_b32 v75, a0
	s_waitcnt lgkmcnt(0)
	s_lshl_b32 s24, s24, 7
	s_mov_b32 s0, 32
	s_mov_b32 s1, 0
	v_mul_lo_u32 v10, v10, s24
	v_mov_b32_e32 v11, 0
	s_mul_i32 s2, s1, s6
	s_mul_i32 s3, s0, s7
	s_add_i32 s4, s3, s2
	v_mad_u64_u32 v[0:1], s[2:3], s0, v0, v[10:11]
	v_or_b32_e32 v0, v0, v8
	v_lshl_or_b32 v77, v8, 1, v76
	v_mul_u32_u24_e32 v8, 40, v4
	s_waitcnt vmcnt(0)
	v_lshl_add_u32 v78, v8, 1, v77
	v_fma_f32 v8, s5, v75, v9
	v_max_f32_e32 v8, 0, v8
	s_mov_b32 s2, 0x43800000
	v_mul_u32_u24_e32 v11, 0xa0, v26
	v_fma_mixlo_f16 v10, v8, s2, 0
	v_or_b32_e32 v11, v11, v24
	v_accvgpr_read_b32 v74, a1
	v_fma_mixlo_f16 v8, v8, s2, -v10 op_sel_hi:[0,0,1]
	v_lshl_or_b32 v26, v11, 1, v76
	s_barrier
	ds_write_b16 v26, v10
	ds_write_b16 v26, v8 offset:5120
	v_fma_f32 v8, s5, v74, v9
	v_max_f32_e32 v8, 0, v8
	v_fma_mixlo_f16 v10, v8, s2, 0
	v_accvgpr_read_b32 v73, a2
	v_fma_mixlo_f16 v8, v8, s2, -v10 op_sel_hi:[0,0,1]
	ds_write_b16 v26, v10 offset:80
	ds_write_b16 v26, v8 offset:5200
	v_fma_f32 v8, s5, v73, v9
	v_max_f32_e32 v8, 0, v8
	v_fma_mixlo_f16 v10, v8, s2, 0
	v_accvgpr_read_b32 v72, a3
	v_fma_mixlo_f16 v8, v8, s2, -v10 op_sel_hi:[0,0,1]
	ds_write_b16 v26, v10 offset:160
	ds_write_b16 v26, v8 offset:5280
	v_fma_f32 v8, s5, v72, v9
	v_max_f32_e32 v8, 0, v8
	v_fma_mixlo_f16 v10, v8, s2, 0
	v_accvgpr_read_b32 v71, a4
	v_fma_mixlo_f16 v8, v8, s2, -v10 op_sel_hi:[0,0,1]
	ds_write_b16 v26, v10 offset:240
	ds_write_b16 v26, v8 offset:5360
	v_fma_f32 v8, s5, v71, v9
	v_max_f32_e32 v8, 0, v8
	v_fma_mixlo_f16 v10, v8, s2, 0
	v_accvgpr_read_b32 v70, a5
	v_fma_mixlo_f16 v8, v8, s2, -v10 op_sel_hi:[0,0,1]
	ds_write_b16 v26, v10 offset:640
	ds_write_b16 v26, v8 offset:5760
	v_fma_f32 v8, s5, v70, v9
	v_max_f32_e32 v8, 0, v8
	v_fma_mixlo_f16 v10, v8, s2, 0
	v_accvgpr_read_b32 v69, a6
	v_fma_mixlo_f16 v8, v8, s2, -v10 op_sel_hi:[0,0,1]
	ds_write_b16 v26, v10 offset:720
	ds_write_b16 v26, v8 offset:5840
	v_fma_f32 v8, s5, v69, v9
	v_max_f32_e32 v8, 0, v8
	v_fma_mixlo_f16 v10, v8, s2, 0
	v_accvgpr_read_b32 v68, a7
	v_fma_mixlo_f16 v8, v8, s2, -v10 op_sel_hi:[0,0,1]
	ds_write_b16 v26, v10 offset:800
	ds_write_b16 v26, v8 offset:5920
	v_fma_f32 v8, s5, v68, v9
	v_max_f32_e32 v8, 0, v8
	v_fma_mixlo_f16 v10, v8, s2, 0
	v_accvgpr_read_b32 v67, a8
	v_fma_mixlo_f16 v8, v8, s2, -v10 op_sel_hi:[0,0,1]
	ds_write_b16 v26, v10 offset:880
	ds_write_b16 v26, v8 offset:6000
	v_fma_f32 v8, s5, v67, v9
	v_max_f32_e32 v8, 0, v8
	v_fma_mixlo_f16 v10, v8, s2, 0
	v_accvgpr_read_b32 v66, a9
	v_fma_mixlo_f16 v8, v8, s2, -v10 op_sel_hi:[0,0,1]
	ds_write_b16 v26, v10 offset:1280
	ds_write_b16 v26, v8 offset:6400
	v_fma_f32 v8, s5, v66, v9
	v_max_f32_e32 v8, 0, v8
	v_fma_mixlo_f16 v10, v8, s2, 0
	v_accvgpr_read_b32 v65, a10
	v_fma_mixlo_f16 v8, v8, s2, -v10 op_sel_hi:[0,0,1]
	ds_write_b16 v26, v10 offset:1360
	ds_write_b16 v26, v8 offset:6480
	v_fma_f32 v8, s5, v65, v9
	v_max_f32_e32 v8, 0, v8
	v_fma_mixlo_f16 v10, v8, s2, 0
	v_accvgpr_read_b32 v64, a11
	v_fma_mixlo_f16 v8, v8, s2, -v10 op_sel_hi:[0,0,1]
	ds_write_b16 v26, v10 offset:1440
	ds_write_b16 v26, v8 offset:6560
	v_fma_f32 v8, s5, v64, v9
	v_max_f32_e32 v8, 0, v8
	v_fma_mixlo_f16 v10, v8, s2, 0
	v_accvgpr_read_b32 v63, a12
	v_fma_mixlo_f16 v8, v8, s2, -v10 op_sel_hi:[0,0,1]
	ds_write_b16 v26, v10 offset:1520
	ds_write_b16 v26, v8 offset:6640
	v_fma_f32 v8, s5, v63, v9
	v_max_f32_e32 v8, 0, v8
	v_fma_mixlo_f16 v10, v8, s2, 0
	v_accvgpr_read_b32 v62, a13
	v_fma_mixlo_f16 v8, v8, s2, -v10 op_sel_hi:[0,0,1]
	ds_write_b16 v26, v10 offset:1920
	ds_write_b16 v26, v8 offset:7040
	v_fma_f32 v8, s5, v62, v9
	v_max_f32_e32 v8, 0, v8
	v_fma_mixlo_f16 v10, v8, s2, 0
	v_accvgpr_read_b32 v61, a14
	v_fma_mixlo_f16 v8, v8, s2, -v10 op_sel_hi:[0,0,1]
	ds_write_b16 v26, v10 offset:2000
	ds_write_b16 v26, v8 offset:7120
	v_fma_f32 v8, s5, v61, v9
	v_max_f32_e32 v8, 0, v8
	v_fma_mixlo_f16 v10, v8, s2, 0
	v_accvgpr_read_b32 v60, a15
	v_fma_mixlo_f16 v8, v8, s2, -v10 op_sel_hi:[0,0,1]
	ds_write_b16 v26, v10 offset:2080
	ds_write_b16 v26, v8 offset:7200
	v_fma_f32 v8, s5, v60, v9
	v_max_f32_e32 v8, 0, v8
	v_fma_mixlo_f16 v10, v8, s2, 0
	v_accvgpr_read_b32 v59, a16
	v_fma_mixlo_f16 v8, v8, s2, -v10 op_sel_hi:[0,0,1]
	ds_write_b16 v26, v10 offset:2160
	ds_write_b16 v26, v8 offset:7280
	v_fma_f32 v8, s5, v59, v9
	v_max_f32_e32 v8, 0, v8
	v_fma_mixlo_f16 v10, v8, s2, 0
	v_accvgpr_read_b32 v58, a17
	v_fma_mixlo_f16 v8, v8, s2, -v10 op_sel_hi:[0,0,1]
	ds_write_b16 v26, v10 offset:2560
	ds_write_b16 v26, v8 offset:7680
	v_fma_f32 v8, s5, v58, v9
	v_max_f32_e32 v8, 0, v8
	v_fma_mixlo_f16 v10, v8, s2, 0
	v_accvgpr_read_b32 v57, a18
	v_fma_mixlo_f16 v8, v8, s2, -v10 op_sel_hi:[0,0,1]
	ds_write_b16 v26, v10 offset:2640
	ds_write_b16 v26, v8 offset:7760
	v_fma_f32 v8, s5, v57, v9
	v_max_f32_e32 v8, 0, v8
	v_fma_mixlo_f16 v10, v8, s2, 0
	v_accvgpr_read_b32 v56, a19
	v_fma_mixlo_f16 v8, v8, s2, -v10 op_sel_hi:[0,0,1]
	ds_write_b16 v26, v10 offset:2720
	ds_write_b16 v26, v8 offset:7840
	v_fma_f32 v8, s5, v56, v9
	v_max_f32_e32 v8, 0, v8
	v_fma_mixlo_f16 v10, v8, s2, 0
	v_accvgpr_read_b32 v55, a20
	v_fma_mixlo_f16 v8, v8, s2, -v10 op_sel_hi:[0,0,1]
	ds_write_b16 v26, v10 offset:2800
	ds_write_b16 v26, v8 offset:7920
	v_fma_f32 v8, s5, v55, v9
	v_max_f32_e32 v8, 0, v8
	v_fma_mixlo_f16 v10, v8, s2, 0
	v_accvgpr_read_b32 v54, a21
	v_fma_mixlo_f16 v8, v8, s2, -v10 op_sel_hi:[0,0,1]
	ds_write_b16 v26, v10 offset:3200
	ds_write_b16 v26, v8 offset:8320
	v_fma_f32 v8, s5, v54, v9
	v_max_f32_e32 v8, 0, v8
	v_fma_mixlo_f16 v10, v8, s2, 0
	v_accvgpr_read_b32 v53, a22
	v_fma_mixlo_f16 v8, v8, s2, -v10 op_sel_hi:[0,0,1]
	ds_write_b16 v26, v10 offset:3280
	ds_write_b16 v26, v8 offset:8400
	v_fma_f32 v8, s5, v53, v9
	v_max_f32_e32 v8, 0, v8
	v_fma_mixlo_f16 v10, v8, s2, 0
	v_accvgpr_read_b32 v52, a23
	v_fma_mixlo_f16 v8, v8, s2, -v10 op_sel_hi:[0,0,1]
	ds_write_b16 v26, v10 offset:3360
	ds_write_b16 v26, v8 offset:8480
	v_fma_f32 v8, s5, v52, v9
	v_max_f32_e32 v8, 0, v8
	v_fma_mixlo_f16 v10, v8, s2, 0
	v_accvgpr_read_b32 v51, a24
	v_fma_mixlo_f16 v8, v8, s2, -v10 op_sel_hi:[0,0,1]
	ds_write_b16 v26, v10 offset:3440
	ds_write_b16 v26, v8 offset:8560
	v_fma_f32 v8, s5, v51, v9
	v_max_f32_e32 v8, 0, v8
	v_fma_mixlo_f16 v10, v8, s2, 0
	v_accvgpr_read_b32 v50, a25
	v_fma_mixlo_f16 v8, v8, s2, -v10 op_sel_hi:[0,0,1]
	ds_write_b16 v26, v10 offset:3840
	ds_write_b16 v26, v8 offset:8960
	v_fma_f32 v8, s5, v50, v9
	v_max_f32_e32 v8, 0, v8
	v_fma_mixlo_f16 v10, v8, s2, 0
	v_accvgpr_read_b32 v49, a26
	v_fma_mixlo_f16 v8, v8, s2, -v10 op_sel_hi:[0,0,1]
	ds_write_b16 v26, v10 offset:3920
	ds_write_b16 v26, v8 offset:9040
	v_fma_f32 v8, s5, v49, v9
	v_max_f32_e32 v8, 0, v8
	v_fma_mixlo_f16 v10, v8, s2, 0
	v_accvgpr_read_b32 v48, a27
	v_fma_mixlo_f16 v8, v8, s2, -v10 op_sel_hi:[0,0,1]
	ds_write_b16 v26, v10 offset:4000
	ds_write_b16 v26, v8 offset:9120
	v_fma_f32 v8, s5, v48, v9
	v_max_f32_e32 v8, 0, v8
	v_fma_mixlo_f16 v10, v8, s2, 0
	v_accvgpr_read_b32 v47, a28
	v_fma_mixlo_f16 v8, v8, s2, -v10 op_sel_hi:[0,0,1]
	ds_write_b16 v26, v10 offset:4080
	ds_write_b16 v26, v8 offset:9200
	v_fma_f32 v8, s5, v47, v9
	v_max_f32_e32 v8, 0, v8
	v_fma_mixlo_f16 v10, v8, s2, 0
	v_accvgpr_read_b32 v46, a29
	v_fma_mixlo_f16 v8, v8, s2, -v10 op_sel_hi:[0,0,1]
	ds_write_b16 v26, v10 offset:4480
	ds_write_b16 v26, v8 offset:9600
	v_fma_f32 v8, s5, v46, v9
	v_max_f32_e32 v8, 0, v8
	v_fma_mixlo_f16 v10, v8, s2, 0
	v_accvgpr_read_b32 v45, a30
	v_fma_mixlo_f16 v8, v8, s2, -v10 op_sel_hi:[0,0,1]
	ds_write_b16 v26, v10 offset:4560
	ds_write_b16 v26, v8 offset:9680
	v_fma_f32 v8, s5, v45, v9
	v_max_f32_e32 v8, 0, v8
	v_fma_mixlo_f16 v10, v8, s2, 0
	v_accvgpr_read_b32 v44, a31
	v_fma_mixlo_f16 v8, v8, s2, -v10 op_sel_hi:[0,0,1]
	ds_write_b16 v26, v10 offset:4640
	ds_write_b16 v26, v8 offset:9760
	v_fma_f32 v8, s5, v44, v9
	v_max_f32_e32 v8, 0, v8
	v_fma_mixlo_f16 v10, v8, s2, 0
	v_fma_mixlo_f16 v8, v8, s2, -v10 op_sel_hi:[0,0,1]
	ds_write_b16 v26, v10 offset:4720
	ds_write_b16 v26, v8 offset:9840
	v_mad_u64_u32 v[10:11], s[6:7], s0, v4, 0
	v_mov_b32_e32 v8, v11
	v_add_u32_e32 v1, s4, v1
	ds_read_b128 v[44:47], v78
	ds_read_b128 v[48:51], v78 offset:5120
	v_mad_u64_u32 v[24:25], s[6:7], s1, v4, v[8:9]
	v_lshlrev_b64 v[0:1], 1, v[0:1]
	v_mov_b32_e32 v11, v24
	v_lshl_add_u64 v[2:3], s[8:9], 0, v[0:1]
	v_lshlrev_b64 v[10:11], 1, v[10:11]
	v_lshl_add_u64 v[0:1], s[10:11], 0, v[0:1]
	v_lshl_add_u64 v[24:25], v[2:3], 0, v[10:11]
	s_waitcnt lgkmcnt(1)
	global_store_dwordx4 v[24:25], v[44:47], off sc1
	v_lshl_add_u64 v[10:11], v[0:1], 0, v[10:11]
	v_or_b32_e32 v24, 16, v4
	s_waitcnt lgkmcnt(0)
	global_store_dwordx4 v[10:11], v[48:51], off sc1
	v_mul_u32_u24_e32 v8, 40, v24
	v_mad_u64_u32 v[10:11], s[6:7], s0, v24, 0
	v_lshl_add_u32 v56, v8, 1, v77
	v_mov_b32_e32 v8, v11
	ds_read_b128 v[44:47], v56
	ds_read_b128 v[48:51], v56 offset:5120
	v_mad_u64_u32 v[24:25], s[6:7], s1, v24, v[8:9]
	v_mov_b32_e32 v11, v24
	v_lshlrev_b64 v[10:11], 1, v[10:11]
	v_lshl_add_u64 v[24:25], v[2:3], 0, v[10:11]
	s_waitcnt lgkmcnt(1)
	global_store_dwordx4 v[24:25], v[44:47], off sc1
	v_lshl_add_u64 v[10:11], v[0:1], 0, v[10:11]
	v_or_b32_e32 v24, 32, v4
	s_waitcnt lgkmcnt(0)
	global_store_dwordx4 v[10:11], v[48:51], off sc1
	v_mad_u64_u32 v[10:11], s[6:7], s0, v24, 0
	ds_read_b128 v[52:55], v56 offset:1280
	ds_read_b128 v[44:47], v56 offset:2560
	v_mov_b32_e32 v8, v11
	ds_read_b128 v[48:51], v56 offset:6400
	v_mad_u64_u32 v[24:25], s[6:7], s1, v24, v[8:9]
	v_mov_b32_e32 v11, v24
	v_lshlrev_b64 v[10:11], 1, v[10:11]
	v_lshl_add_u64 v[24:25], v[2:3], 0, v[10:11]
	s_waitcnt lgkmcnt(2)
	global_store_dwordx4 v[24:25], v[52:55], off sc1
	v_lshl_add_u64 v[10:11], v[0:1], 0, v[10:11]
	v_or_b32_e32 v24, 48, v4
	ds_read_b128 v[52:55], v56 offset:7680
	s_waitcnt lgkmcnt(1)
	global_store_dwordx4 v[10:11], v[48:51], off sc1
	v_mad_u64_u32 v[10:11], s[6:7], s0, v24, 0
	v_mov_b32_e32 v8, v11
	v_mad_u64_u32 v[24:25], s[6:7], s1, v24, v[8:9]
	v_accvgpr_read_b32 v43, a32
	v_mov_b32_e32 v11, v24
	v_lshlrev_b64 v[10:11], 1, v[10:11]
	v_fma_f32 v8, s5, v43, v9
	v_lshl_add_u64 v[24:25], v[2:3], 0, v[10:11]
	v_lshl_add_u64 v[10:11], v[0:1], 0, v[10:11]
	v_max_f32_e32 v8, 0, v8
	s_waitcnt lgkmcnt(0)
	global_store_dwordx4 v[10:11], v[52:55], off sc1
	v_fma_mixlo_f16 v10, v8, s2, 0
	v_accvgpr_read_b32 v42, a33
	v_fma_mixlo_f16 v8, v8, s2, -v10 op_sel_hi:[0,0,1]
	global_store_dwordx4 v[24:25], v[44:47], off sc1
	ds_write_b16 v26, v10
	ds_write_b16 v26, v8 offset:5120
	v_fma_f32 v8, s5, v42, v9
	v_max_f32_e32 v8, 0, v8
	v_fma_mixlo_f16 v10, v8, s2, 0
	v_accvgpr_read_b32 v41, a34
	v_fma_mixlo_f16 v8, v8, s2, -v10 op_sel_hi:[0,0,1]
	ds_write_b16 v26, v10 offset:80
	ds_write_b16 v26, v8 offset:5200
	v_fma_f32 v8, s5, v41, v9
	v_max_f32_e32 v8, 0, v8
	v_fma_mixlo_f16 v10, v8, s2, 0
	v_accvgpr_read_b32 v40, a35
	v_fma_mixlo_f16 v8, v8, s2, -v10 op_sel_hi:[0,0,1]
	ds_write_b16 v26, v10 offset:160
	ds_write_b16 v26, v8 offset:5280
	v_fma_f32 v8, s5, v40, v9
	v_max_f32_e32 v8, 0, v8
	v_fma_mixlo_f16 v10, v8, s2, 0
	v_accvgpr_read_b32 v39, a36
	v_fma_mixlo_f16 v8, v8, s2, -v10 op_sel_hi:[0,0,1]
	ds_write_b16 v26, v10 offset:240
	ds_write_b16 v26, v8 offset:5360
	v_fma_f32 v8, s5, v39, v9
	v_max_f32_e32 v8, 0, v8
	v_fma_mixlo_f16 v10, v8, s2, 0
	v_accvgpr_read_b32 v38, a37
	v_fma_mixlo_f16 v8, v8, s2, -v10 op_sel_hi:[0,0,1]
	ds_write_b16 v26, v10 offset:640
	ds_write_b16 v26, v8 offset:5760
	v_fma_f32 v8, s5, v38, v9
	v_max_f32_e32 v8, 0, v8
	v_fma_mixlo_f16 v10, v8, s2, 0
	v_accvgpr_read_b32 v37, a38
	v_fma_mixlo_f16 v8, v8, s2, -v10 op_sel_hi:[0,0,1]
	ds_write_b16 v26, v10 offset:720
	ds_write_b16 v26, v8 offset:5840
	v_fma_f32 v8, s5, v37, v9
	v_max_f32_e32 v8, 0, v8
	v_fma_mixlo_f16 v10, v8, s2, 0
	v_accvgpr_read_b32 v36, a39
	v_fma_mixlo_f16 v8, v8, s2, -v10 op_sel_hi:[0,0,1]
	ds_write_b16 v26, v10 offset:800
	ds_write_b16 v26, v8 offset:5920
	v_fma_f32 v8, s5, v36, v9
	v_max_f32_e32 v8, 0, v8
	v_fma_mixlo_f16 v10, v8, s2, 0
	v_accvgpr_read_b32 v35, a40
	v_fma_mixlo_f16 v8, v8, s2, -v10 op_sel_hi:[0,0,1]
	ds_write_b16 v26, v10 offset:880
	ds_write_b16 v26, v8 offset:6000
	v_fma_f32 v8, s5, v35, v9
	v_max_f32_e32 v8, 0, v8
	v_fma_mixlo_f16 v10, v8, s2, 0
	v_accvgpr_read_b32 v34, a41
	v_fma_mixlo_f16 v8, v8, s2, -v10 op_sel_hi:[0,0,1]
	ds_write_b16 v26, v10 offset:1280
	ds_write_b16 v26, v8 offset:6400
	v_fma_f32 v8, s5, v34, v9
	v_max_f32_e32 v8, 0, v8
	v_fma_mixlo_f16 v10, v8, s2, 0
	v_accvgpr_read_b32 v33, a42
	v_fma_mixlo_f16 v8, v8, s2, -v10 op_sel_hi:[0,0,1]
	ds_write_b16 v26, v10 offset:1360
	ds_write_b16 v26, v8 offset:6480
	v_fma_f32 v8, s5, v33, v9
	v_max_f32_e32 v8, 0, v8
	v_fma_mixlo_f16 v10, v8, s2, 0
	v_accvgpr_read_b32 v32, a43
	v_fma_mixlo_f16 v8, v8, s2, -v10 op_sel_hi:[0,0,1]
	ds_write_b16 v26, v10 offset:1440
	ds_write_b16 v26, v8 offset:6560
	v_fma_f32 v8, s5, v32, v9
	v_max_f32_e32 v8, 0, v8
	v_fma_mixlo_f16 v10, v8, s2, 0
	v_accvgpr_read_b32 v31, a44
	v_fma_mixlo_f16 v8, v8, s2, -v10 op_sel_hi:[0,0,1]
	ds_write_b16 v26, v10 offset:1520
	ds_write_b16 v26, v8 offset:6640
	v_fma_f32 v8, s5, v31, v9
	v_max_f32_e32 v8, 0, v8
	v_fma_mixlo_f16 v10, v8, s2, 0
	v_accvgpr_read_b32 v30, a45
	v_fma_mixlo_f16 v8, v8, s2, -v10 op_sel_hi:[0,0,1]
	ds_write_b16 v26, v10 offset:1920
	ds_write_b16 v26, v8 offset:7040
	v_fma_f32 v8, s5, v30, v9
	v_max_f32_e32 v8, 0, v8
	v_fma_mixlo_f16 v10, v8, s2, 0
	v_accvgpr_read_b32 v29, a46
	v_fma_mixlo_f16 v8, v8, s2, -v10 op_sel_hi:[0,0,1]
	ds_write_b16 v26, v10 offset:2000
	ds_write_b16 v26, v8 offset:7120
	v_fma_f32 v8, s5, v29, v9
	v_max_f32_e32 v8, 0, v8
	v_fma_mixlo_f16 v10, v8, s2, 0
	v_accvgpr_read_b32 v28, a47
	v_fma_mixlo_f16 v8, v8, s2, -v10 op_sel_hi:[0,0,1]
	ds_write_b16 v26, v10 offset:2080
	ds_write_b16 v26, v8 offset:7200
	v_fma_f32 v8, s5, v28, v9
	v_max_f32_e32 v8, 0, v8
	v_fma_mixlo_f16 v10, v8, s2, 0
	v_accvgpr_read_b32 v27, a48
	v_fma_mixlo_f16 v8, v8, s2, -v10 op_sel_hi:[0,0,1]
	ds_write_b16 v26, v10 offset:2160
	ds_write_b16 v26, v8 offset:7280
	v_fma_f32 v8, s5, v27, v9
	v_max_f32_e32 v8, 0, v8
	v_fma_mixlo_f16 v10, v8, s2, 0
	v_accvgpr_read_b32 v23, a49
	v_fma_mixlo_f16 v8, v8, s2, -v10 op_sel_hi:[0,0,1]
	ds_write_b16 v26, v10 offset:2560
	ds_write_b16 v26, v8 offset:7680
	v_fma_f32 v8, s5, v23, v9
	v_max_f32_e32 v8, 0, v8
	v_fma_mixlo_f16 v10, v8, s2, 0
	v_accvgpr_read_b32 v22, a50
	v_fma_mixlo_f16 v8, v8, s2, -v10 op_sel_hi:[0,0,1]
	ds_write_b16 v26, v10 offset:2640
	ds_write_b16 v26, v8 offset:7760
	v_fma_f32 v8, s5, v22, v9
	v_max_f32_e32 v8, 0, v8
	v_fma_mixlo_f16 v10, v8, s2, 0
	v_accvgpr_read_b32 v21, a51
	v_fma_mixlo_f16 v8, v8, s2, -v10 op_sel_hi:[0,0,1]
	ds_write_b16 v26, v10 offset:2720
	ds_write_b16 v26, v8 offset:7840
	v_fma_f32 v8, s5, v21, v9
	v_max_f32_e32 v8, 0, v8
	v_fma_mixlo_f16 v10, v8, s2, 0
	v_accvgpr_read_b32 v20, a52
	v_fma_mixlo_f16 v8, v8, s2, -v10 op_sel_hi:[0,0,1]
	ds_write_b16 v26, v10 offset:2800
	ds_write_b16 v26, v8 offset:7920
	v_fma_f32 v8, s5, v20, v9
	v_max_f32_e32 v8, 0, v8
	v_fma_mixlo_f16 v10, v8, s2, 0
	v_accvgpr_read_b32 v19, a53
	v_fma_mixlo_f16 v8, v8, s2, -v10 op_sel_hi:[0,0,1]
	ds_write_b16 v26, v10 offset:3200
	ds_write_b16 v26, v8 offset:8320
	v_fma_f32 v8, s5, v19, v9
	v_max_f32_e32 v8, 0, v8
	v_fma_mixlo_f16 v10, v8, s2, 0
	v_accvgpr_read_b32 v18, a54
	v_fma_mixlo_f16 v8, v8, s2, -v10 op_sel_hi:[0,0,1]
	ds_write_b16 v26, v10 offset:3280
	ds_write_b16 v26, v8 offset:8400
	v_fma_f32 v8, s5, v18, v9
	v_max_f32_e32 v8, 0, v8
	v_fma_mixlo_f16 v10, v8, s2, 0
	v_accvgpr_read_b32 v17, a55
	v_fma_mixlo_f16 v8, v8, s2, -v10 op_sel_hi:[0,0,1]
	ds_write_b16 v26, v10 offset:3360
	ds_write_b16 v26, v8 offset:8480
	v_fma_f32 v8, s5, v17, v9
	v_max_f32_e32 v8, 0, v8
	v_fma_mixlo_f16 v10, v8, s2, 0
	v_accvgpr_read_b32 v16, a56
	v_fma_mixlo_f16 v8, v8, s2, -v10 op_sel_hi:[0,0,1]
	ds_write_b16 v26, v10 offset:3440
	ds_write_b16 v26, v8 offset:8560
	v_fma_f32 v8, s5, v16, v9
	v_max_f32_e32 v8, 0, v8
	v_fma_mixlo_f16 v10, v8, s2, 0
	v_accvgpr_read_b32 v15, a57
	v_fma_mixlo_f16 v8, v8, s2, -v10 op_sel_hi:[0,0,1]
	ds_write_b16 v26, v10 offset:3840
	ds_write_b16 v26, v8 offset:8960
	v_fma_f32 v8, s5, v15, v9
	v_max_f32_e32 v8, 0, v8
	v_fma_mixlo_f16 v10, v8, s2, 0
	v_accvgpr_read_b32 v14, a58
	v_fma_mixlo_f16 v8, v8, s2, -v10 op_sel_hi:[0,0,1]
	ds_write_b16 v26, v10 offset:3920
	ds_write_b16 v26, v8 offset:9040
	v_fma_f32 v8, s5, v14, v9
	v_max_f32_e32 v8, 0, v8
	v_fma_mixlo_f16 v10, v8, s2, 0
	v_accvgpr_read_b32 v13, a59
	v_fma_mixlo_f16 v8, v8, s2, -v10 op_sel_hi:[0,0,1]
	ds_write_b16 v26, v10 offset:4000
	ds_write_b16 v26, v8 offset:9120
	v_fma_f32 v8, s5, v13, v9
	v_max_f32_e32 v8, 0, v8
	v_fma_mixlo_f16 v10, v8, s2, 0
	v_accvgpr_read_b32 v12, a60
	v_fma_mixlo_f16 v8, v8, s2, -v10 op_sel_hi:[0,0,1]
	ds_write_b16 v26, v10 offset:4080
	ds_write_b16 v26, v8 offset:9200
	v_fma_f32 v8, s5, v12, v9
	v_accvgpr_read_b32 v7, a61
	v_max_f32_e32 v8, 0, v8
	v_fma_mixlo_f16 v10, v8, s2, 0
	v_fma_f32 v7, s5, v7, v9
	v_accvgpr_read_b32 v6, a62
	v_fma_mixlo_f16 v8, v8, s2, -v10 op_sel_hi:[0,0,1]
	v_max_f32_e32 v7, 0, v7
	ds_write_b16 v26, v10 offset:4480
	ds_write_b16 v26, v8 offset:9600
	v_fma_mixlo_f16 v8, v7, s2, 0
	v_fma_f32 v6, s5, v6, v9
	v_accvgpr_read_b32 v5, a63
	v_fma_mixlo_f16 v7, v7, s2, -v8 op_sel_hi:[0,0,1]
	v_max_f32_e32 v6, 0, v6
	ds_write_b16 v26, v8 offset:4560
	ds_write_b16 v26, v7 offset:9680
	v_fma_mixlo_f16 v7, v6, s2, 0
	v_fmac_f32_e32 v9, s5, v5
	v_fma_mixlo_f16 v6, v6, s2, -v7 op_sel_hi:[0,0,1]
	v_max_f32_e32 v5, 0, v9
	ds_write_b16 v26, v7 offset:4640
	ds_write_b16 v26, v6 offset:9760
	v_fma_mixlo_f16 v6, v5, s2, 0
	v_fma_mixlo_f16 v5, v5, s2, -v6 op_sel_hi:[0,0,1]
	ds_write_b16 v26, v6 offset:4720
	ds_write_b16 v26, v5 offset:9840
	v_or_b32_e32 v5, 64, v4
	v_mad_u64_u32 v[14:15], s[2:3], s0, v5, 0
	v_mov_b32_e32 v16, v15
	ds_read_b128 v[6:9], v78
	ds_read_b128 v[10:13], v78 offset:5120
	v_mad_u64_u32 v[16:17], s[2:3], s1, v5, v[16:17]
	v_mov_b32_e32 v15, v16
	v_lshlrev_b64 v[14:15], 1, v[14:15]
	v_lshl_add_u64 v[16:17], v[2:3], 0, v[14:15]
	s_waitcnt lgkmcnt(1)
	global_store_dwordx4 v[16:17], v[6:9], off sc1
	v_or_b32_e32 v5, 0x50, v4
	s_nop 0
	v_lshl_add_u64 v[6:7], v[0:1], 0, v[14:15]
	s_waitcnt lgkmcnt(0)
	global_store_dwordx4 v[6:7], v[10:13], off sc1
	v_mad_u64_u32 v[14:15], s[2:3], s0, v5, 0
	ds_read_b128 v[6:9], v56
	ds_read_b128 v[10:13], v56 offset:5120
	v_mov_b32_e32 v16, v15
	v_mad_u64_u32 v[16:17], s[2:3], s1, v5, v[16:17]
	v_mov_b32_e32 v15, v16
	v_lshlrev_b64 v[18:19], 1, v[14:15]
	v_lshl_add_u64 v[20:21], v[2:3], 0, v[18:19]
	v_lshl_add_u64 v[18:19], v[0:1], 0, v[18:19]
	v_or_b32_e32 v5, 0x60, v4
	s_waitcnt lgkmcnt(0)
	global_store_dwordx4 v[18:19], v[10:13], off sc1
	v_mad_u64_u32 v[18:19], s[2:3], s0, v5, 0
	ds_read_b128 v[14:17], v56 offset:1280
	global_store_dwordx4 v[20:21], v[6:9], off sc1
	ds_read_b128 v[10:13], v56 offset:6400
	v_mov_b32_e32 v20, v19
	v_mad_u64_u32 v[20:21], s[2:3], s1, v5, v[20:21]
	v_mov_b32_e32 v19, v20
	v_lshlrev_b64 v[18:19], 1, v[18:19]
	v_lshl_add_u64 v[20:21], v[2:3], 0, v[18:19]
	v_lshl_add_u64 v[18:19], v[0:1], 0, v[18:19]
	ds_read_b128 v[6:9], v56 offset:2560
	s_waitcnt lgkmcnt(2)
	global_store_dwordx4 v[20:21], v[14:17], off sc1
	ds_read_b128 v[14:17], v56 offset:7680
	s_waitcnt lgkmcnt(2)
	global_store_dwordx4 v[18:19], v[10:13], off sc1
	s_nop 1
	v_or_b32_e32 v11, 0x70, v4
	v_mad_u64_u32 v[4:5], s[2:3], s0, v11, 0
	v_mov_b32_e32 v10, v5
	v_mad_u64_u32 v[10:11], s[0:1], s1, v11, v[10:11]
	v_mov_b32_e32 v5, v10
	v_lshlrev_b64 v[4:5], 1, v[4:5]
	v_lshl_add_u64 v[2:3], v[2:3], 0, v[4:5]
	v_lshl_add_u64 v[0:1], v[0:1], 0, v[4:5]
	s_waitcnt lgkmcnt(1)
	global_store_dwordx4 v[2:3], v[6:9], off sc1
	s_waitcnt lgkmcnt(0)
	global_store_dwordx4 v[0:1], v[14:17], off sc1
	s_endpgm
	s_endpgm
	s_endpgm
	s_endpgm
	s_endpgm
	s_endpgm
	s_endpgm
	s_endpgm
	s_endpgm
	s_endpgm
	s_endpgm
	s_endpgm
	s_endpgm
	s_endpgm
	s_endpgm
	s_endpgm
	s_endpgm
	s_endpgm
	s_endpgm
	s_endpgm
	s_endpgm
	s_endpgm
	s_endpgm
	s_endpgm
	s_endpgm
	s_endpgm
	s_endpgm
	s_endpgm
	s_endpgm
	s_endpgm
	s_endpgm
	s_endpgm
	s_endpgm
	s_endpgm
	s_endpgm
	s_endpgm
	s_endpgm
	s_endpgm
	s_endpgm
	s_endpgm
	s_endpgm
	s_endpgm
	s_endpgm
	s_endpgm
	s_endpgm
	s_endpgm
	s_endpgm
	s_endpgm
	s_endpgm
	s_endpgm
	s_endpgm
	s_endpgm
	s_endpgm
	s_endpgm
	s_endpgm
	s_endpgm
